# load ladders de-serialised: softmax epilogue's 8 RSS loads issued together with counted waits; phase-0 tile's 16 gain loads issued together at the tile head
# speedup vs baseline: 1.0020x; 1.0011x over previous
.LBB0_118:
	s_lshr_b32 s90, s18, 8
	v_cvt_f32_u32_e32 v66, s90
	s_sub_i32 s15, 0, s90
	s_abs_i32 s14, s1
	s_ashr_i32 s2, s1, 31
	v_rcp_iflag_f32_e32 v66, v66
	s_nop 0
	v_mul_f32_e32 v66, 0x4f7ffffe, v66
	v_cvt_u32_f32_e32 v66, v66
	s_nop 0
	v_readfirstlane_b32 s20, v66
	s_mul_i32 s15, s15, s20
	s_mul_hi_u32 s15, s20, s15
	s_add_i32 s20, s20, s15
	s_mul_hi_u32 s15, s14, s20
	s_mul_i32 s20, s15, s90
	s_sub_i32 s14, s14, s20
	s_add_i32 s21, s15, 1
	s_sub_i32 s20, s14, s90
	s_cmp_ge_u32 s14, s90
	s_cselect_b32 s15, s21, s15
	s_cselect_b32 s14, s20, s14
	s_add_i32 s20, s15, 1
	s_cmp_ge_u32 s14, s90
	s_cselect_b32 s14, s20, s15
	s_xor_b32 s14, s14, s2
	s_sub_i32 s14, s14, s2
	s_lshl_b32 s2, s14, 7
	s_cmp_eq_u64 s[26:27], 0
	s_cbranch_scc1 .Lcvt_gain_none
	v_add_u32_e32 v168, s2, v74
	v_ashrrev_i32_e32 v169, 31, v168
	v_lshl_add_u64 v[168:169], v[168:169], 2, s[26:27]
	global_load_dword v136, v[168:169], off
	v_add_u32_e32 v170, s2, v75
	v_ashrrev_i32_e32 v171, 31, v170
	v_lshl_add_u64 v[170:171], v[170:171], 2, s[26:27]
	global_load_dword v138, v[170:171], off
	v_add_u32_e32 v168, s2, v76
	v_ashrrev_i32_e32 v169, 31, v168
	v_lshl_add_u64 v[168:169], v[168:169], 2, s[26:27]
	global_load_dword v140, v[168:169], off
	v_add_u32_e32 v170, s2, v77
	v_ashrrev_i32_e32 v171, 31, v170
	v_lshl_add_u64 v[170:171], v[170:171], 2, s[26:27]
	global_load_dword v142, v[170:171], off
	v_add_u32_e32 v168, s2, v78
	v_ashrrev_i32_e32 v169, 31, v168
	v_lshl_add_u64 v[168:169], v[168:169], 2, s[26:27]
	global_load_dword v144, v[168:169], off
	v_add_u32_e32 v170, s2, v79
	v_ashrrev_i32_e32 v171, 31, v170
	v_lshl_add_u64 v[170:171], v[170:171], 2, s[26:27]
	global_load_dword v146, v[170:171], off
	v_add_u32_e32 v168, s2, v80
	v_ashrrev_i32_e32 v169, 31, v168
	v_lshl_add_u64 v[168:169], v[168:169], 2, s[26:27]
	global_load_dword v148, v[168:169], off
	v_add_u32_e32 v170, s2, v81
	v_ashrrev_i32_e32 v171, 31, v170
	v_lshl_add_u64 v[170:171], v[170:171], 2, s[26:27]
	global_load_dword v150, v[170:171], off
	v_add_u32_e32 v168, s2, v82
	v_ashrrev_i32_e32 v169, 31, v168
	v_lshl_add_u64 v[168:169], v[168:169], 2, s[26:27]
	global_load_dword v152, v[168:169], off
	v_add_u32_e32 v170, s2, v83
	v_ashrrev_i32_e32 v171, 31, v170
	v_lshl_add_u64 v[170:171], v[170:171], 2, s[26:27]
	global_load_dword v154, v[170:171], off
	v_add_u32_e32 v168, s2, v84
	v_ashrrev_i32_e32 v169, 31, v168
	v_lshl_add_u64 v[168:169], v[168:169], 2, s[26:27]
	global_load_dword v156, v[168:169], off
	v_add_u32_e32 v170, s2, v85
	v_ashrrev_i32_e32 v171, 31, v170
	v_lshl_add_u64 v[170:171], v[170:171], 2, s[26:27]
	global_load_dword v158, v[170:171], off
	v_add_u32_e32 v168, s2, v86
	v_ashrrev_i32_e32 v169, 31, v168
	v_lshl_add_u64 v[168:169], v[168:169], 2, s[26:27]
	global_load_dword v160, v[168:169], off
	v_add_u32_e32 v170, s2, v87
	v_ashrrev_i32_e32 v171, 31, v170
	v_lshl_add_u64 v[170:171], v[170:171], 2, s[26:27]
	global_load_dword v162, v[170:171], off
	v_add_u32_e32 v168, s2, v88
	v_ashrrev_i32_e32 v169, 31, v168
	v_lshl_add_u64 v[168:169], v[168:169], 2, s[26:27]
	global_load_dword v164, v[168:169], off
	v_add_u32_e32 v170, s2, v89
	v_ashrrev_i32_e32 v171, 31, v170
	v_lshl_add_u64 v[170:171], v[170:171], 2, s[26:27]
	global_load_dword v166, v[170:171], off
.Lcvt_gain_none:
	s_cmp_lg_u64 s[26:27], 0
	s_waitcnt vmcnt(0)
	v_mov_b64_e32 v[68:69], v[8:9]
	s_cselect_b64 s[66:67], -1, 0
	s_cmp_eq_u64 s[26:27], 0
	v_mov_b64_e32 v[66:67], v[6:7]
	s_cbranch_scc1 .LBB0_120
	v_pk_mul_f32 v[68:69], v[8:9], v[136:137] op_sel_hi:[1,0]
	v_pk_mul_f32 v[66:67], v[6:7], v[136:137] op_sel_hi:[1,0]
.LBB0_120:
	s_mul_i32 s21, s11, 0x10400
	s_add_i32 s15, s21, 0
	v_add_u32_e32 v111, s15, v90
	v_cvt_pk_bf16_f32 v66, v66, v67
	v_cvt_pk_bf16_f32 v67, v68, v69
	v_add_u32_e32 v68, v111, v91
	ds_write_b64 v68, v[66:67]
	v_cndmask_b32_e64 v66, 0, 1, s[66:67]
	v_cmp_ne_u32_e64 s[36:37], 1, v66
	v_mov_b64_e32 v[68:69], v[4:5]
	s_andn2_b64 vcc, exec, s[66:67]
	v_mov_b64_e32 v[66:67], v[2:3]
	s_cbranch_vccnz .LBB0_122
	v_pk_mul_f32 v[68:69], v[4:5], v[138:139] op_sel_hi:[1,0]
	v_pk_mul_f32 v[66:67], v[2:3], v[138:139] op_sel_hi:[1,0]
.LBB0_122:
	s_nop 0
	v_cvt_pk_bf16_f32 v66, v66, v67
	v_cvt_pk_bf16_f32 v67, v68, v69
	v_add_u32_e32 v68, v111, v92
	ds_write_b64 v68, v[66:67]
	v_mov_b64_e32 v[68:69], v[16:17]
	s_and_b64 vcc, exec, s[36:37]
	v_mov_b64_e32 v[66:67], v[14:15]
	s_cbranch_vccnz .LBB0_124
	v_pk_mul_f32 v[68:69], v[16:17], v[140:141] op_sel_hi:[1,0]
	v_pk_mul_f32 v[66:67], v[14:15], v[140:141] op_sel_hi:[1,0]
.LBB0_124:
	s_nop 0
	v_cvt_pk_bf16_f32 v66, v66, v67
	v_cvt_pk_bf16_f32 v67, v68, v69
	v_add_u32_e32 v68, v111, v93
	ds_write_b64 v68, v[66:67]
	v_mov_b64_e32 v[68:69], v[12:13]
	s_and_b64 vcc, exec, s[36:37]
	v_mov_b64_e32 v[66:67], v[10:11]
	s_cbranch_vccnz .LBB0_126
	v_pk_mul_f32 v[68:69], v[12:13], v[142:143] op_sel_hi:[1,0]
	v_pk_mul_f32 v[66:67], v[10:11], v[142:143] op_sel_hi:[1,0]
.LBB0_126:
	s_nop 0
	v_cvt_pk_bf16_f32 v66, v66, v67
	v_cvt_pk_bf16_f32 v67, v68, v69
	v_add_u32_e32 v68, v111, v94
	ds_write_b64 v68, v[66:67]
	v_mov_b64_e32 v[68:69], v[24:25]
	s_and_b64 vcc, exec, s[36:37]
	v_mov_b64_e32 v[66:67], v[22:23]
	s_cbranch_vccnz .LBB0_128
	v_pk_mul_f32 v[68:69], v[24:25], v[144:145] op_sel_hi:[1,0]
	v_pk_mul_f32 v[66:67], v[22:23], v[144:145] op_sel_hi:[1,0]
.LBB0_128:
	s_nop 0
	v_cvt_pk_bf16_f32 v66, v66, v67
	v_cvt_pk_bf16_f32 v67, v68, v69
	v_add_u32_e32 v68, v111, v95
	ds_write_b64 v68, v[66:67]
	v_mov_b64_e32 v[68:69], v[20:21]
	s_and_b64 vcc, exec, s[36:37]
	v_mov_b64_e32 v[66:67], v[18:19]
	s_cbranch_vccnz .LBB0_130
	v_pk_mul_f32 v[68:69], v[20:21], v[146:147] op_sel_hi:[1,0]
	v_pk_mul_f32 v[66:67], v[18:19], v[146:147] op_sel_hi:[1,0]
.LBB0_130:
	s_nop 0
	v_cvt_pk_bf16_f32 v66, v66, v67
	v_cvt_pk_bf16_f32 v67, v68, v69
	v_add_u32_e32 v68, v111, v96
	ds_write_b64 v68, v[66:67]
	v_mov_b64_e32 v[68:69], v[32:33]
	s_and_b64 vcc, exec, s[36:37]
	v_mov_b64_e32 v[66:67], v[30:31]
	s_cbranch_vccnz .LBB0_132
	v_pk_mul_f32 v[68:69], v[32:33], v[148:149] op_sel_hi:[1,0]
	v_pk_mul_f32 v[66:67], v[30:31], v[148:149] op_sel_hi:[1,0]
.LBB0_132:
	s_nop 0
	v_cvt_pk_bf16_f32 v66, v66, v67
	v_cvt_pk_bf16_f32 v67, v68, v69
	v_add_u32_e32 v68, v111, v97
	ds_write_b64 v68, v[66:67]
	v_mov_b64_e32 v[68:69], v[28:29]
	s_and_b64 vcc, exec, s[36:37]
	v_mov_b64_e32 v[66:67], v[26:27]
	s_cbranch_vccnz .LBB0_134
	v_pk_mul_f32 v[68:69], v[28:29], v[150:151] op_sel_hi:[1,0]
	v_pk_mul_f32 v[66:67], v[26:27], v[150:151] op_sel_hi:[1,0]
.LBB0_134:
	s_nop 0
	v_cvt_pk_bf16_f32 v66, v66, v67
	v_cvt_pk_bf16_f32 v67, v68, v69
	v_add_u32_e32 v68, v111, v101
	ds_write_b64 v68, v[66:67]
	v_mov_b64_e32 v[68:69], v[40:41]
	s_and_b64 vcc, exec, s[36:37]
	v_mov_b64_e32 v[66:67], v[38:39]
	s_cbranch_vccnz .LBB0_136
	v_pk_mul_f32 v[68:69], v[40:41], v[152:153] op_sel_hi:[1,0]
	v_pk_mul_f32 v[66:67], v[38:39], v[152:153] op_sel_hi:[1,0]
.LBB0_136:
	s_nop 0
	v_cvt_pk_bf16_f32 v66, v66, v67
	v_cvt_pk_bf16_f32 v67, v68, v69
	v_add_u32_e32 v68, v111, v102
	ds_write_b64 v68, v[66:67]
	v_mov_b64_e32 v[68:69], v[36:37]
	s_and_b64 vcc, exec, s[36:37]
	v_mov_b64_e32 v[66:67], v[34:35]
	s_cbranch_vccnz .LBB0_138
	v_pk_mul_f32 v[68:69], v[36:37], v[154:155] op_sel_hi:[1,0]
	v_pk_mul_f32 v[66:67], v[34:35], v[154:155] op_sel_hi:[1,0]
.LBB0_138:
	s_nop 0
	v_cvt_pk_bf16_f32 v66, v66, v67
	v_cvt_pk_bf16_f32 v67, v68, v69
	v_add_u32_e32 v68, v111, v103
	ds_write_b64 v68, v[66:67]
	v_mov_b64_e32 v[68:69], v[48:49]
	s_and_b64 vcc, exec, s[36:37]
	v_mov_b64_e32 v[66:67], v[46:47]
	s_cbranch_vccnz .LBB0_140
	v_pk_mul_f32 v[68:69], v[48:49], v[156:157] op_sel_hi:[1,0]
	v_pk_mul_f32 v[66:67], v[46:47], v[156:157] op_sel_hi:[1,0]
.LBB0_140:
	s_nop 0
	v_cvt_pk_bf16_f32 v66, v66, v67
	v_cvt_pk_bf16_f32 v67, v68, v69
	v_add_u32_e32 v68, v111, v104
	ds_write_b64 v68, v[66:67]
	v_mov_b64_e32 v[68:69], v[44:45]
	s_and_b64 vcc, exec, s[36:37]
	v_mov_b64_e32 v[66:67], v[42:43]
	s_cbranch_vccnz .LBB0_142
	v_pk_mul_f32 v[68:69], v[44:45], v[158:159] op_sel_hi:[1,0]
	v_pk_mul_f32 v[66:67], v[42:43], v[158:159] op_sel_hi:[1,0]
.LBB0_142:
	s_nop 0
	v_cvt_pk_bf16_f32 v66, v66, v67
	v_cvt_pk_bf16_f32 v67, v68, v69
	v_add_u32_e32 v68, v111, v105
	ds_write_b64 v68, v[66:67]
	v_mov_b64_e32 v[68:69], v[56:57]
	s_and_b64 vcc, exec, s[36:37]
	v_mov_b64_e32 v[66:67], v[54:55]
	s_cbranch_vccnz .LBB0_144
	v_pk_mul_f32 v[68:69], v[56:57], v[160:161] op_sel_hi:[1,0]
	v_pk_mul_f32 v[66:67], v[54:55], v[160:161] op_sel_hi:[1,0]
.LBB0_144:
	s_nop 0
	v_cvt_pk_bf16_f32 v66, v66, v67
	v_cvt_pk_bf16_f32 v67, v68, v69
	v_add_u32_e32 v68, v111, v106
	ds_write_b64 v68, v[66:67]
	v_mov_b64_e32 v[68:69], v[52:53]
	s_and_b64 vcc, exec, s[36:37]
	v_mov_b64_e32 v[66:67], v[50:51]
	s_cbranch_vccnz .LBB0_146
	v_pk_mul_f32 v[68:69], v[52:53], v[162:163] op_sel_hi:[1,0]
	v_pk_mul_f32 v[66:67], v[50:51], v[162:163] op_sel_hi:[1,0]
.LBB0_146:
	s_nop 0
	v_cvt_pk_bf16_f32 v66, v66, v67
	v_cvt_pk_bf16_f32 v67, v68, v69
	v_add_u32_e32 v68, v111, v107
	ds_write_b64 v68, v[66:67]
	v_mov_b64_e32 v[68:69], v[64:65]
	s_and_b64 vcc, exec, s[36:37]
	v_mov_b64_e32 v[66:67], v[62:63]
	s_cbranch_vccnz .LBB0_148
	v_pk_mul_f32 v[68:69], v[64:65], v[164:165] op_sel_hi:[1,0]
	v_pk_mul_f32 v[66:67], v[62:63], v[164:165] op_sel_hi:[1,0]
.LBB0_148:
	s_nop 0
	v_cvt_pk_bf16_f32 v66, v66, v67
	v_cvt_pk_bf16_f32 v67, v68, v69
	v_add_u32_e32 v68, v111, v108
	ds_write_b64 v68, v[66:67]
	v_mov_b64_e32 v[68:69], v[60:61]
	s_and_b64 vcc, exec, s[36:37]
	v_mov_b64_e32 v[66:67], v[58:59]
	s_cbranch_vccnz .LBB0_150
	v_pk_mul_f32 v[68:69], v[60:61], v[166:167] op_sel_hi:[1,0]
	v_pk_mul_f32 v[66:67], v[58:59], v[166:167] op_sel_hi:[1,0]

.LBB0_970:
	v_mbcnt_lo_u32_b32 v135, -1, 0
	v_mbcnt_hi_u32_b32 v135, -1, v135
	s_movk_i32 s26, 0x80
	v_and_b32_e32 v132, 15, v135
	v_ashrrev_i32_e32 v131, 4, v135
	v_lshlrev_b32_e32 v134, 6, v131
	v_lshlrev_b32_e32 v136, 2, v132
	v_or_b32_e32 v132, s64, v132
	v_bitop3_b32 v133, v134, 64, v136 bitop3:0x36
	v_bitop3_b32 v220, v134, s26, v136 bitop3:0x36
	v_lshl_add_u32 v134, s21, 8, v132
	v_lshlrev_b32_e32 v222, 4, v132
	v_cmp_gt_u32_e32 vcc, 16, v135
	v_ashrrev_i32_e32 v135, 31, v134
	v_or_b32_e32 v221, s67, v222
	v_lshl_add_u64 v[134:135], v[134:135], 3, s[46:47]
	global_load_dwordx2 v[194:195], v[134:135], off
	global_load_dwordx2 v[196:197], v[134:135], off offset:128
	global_load_dwordx2 v[198:199], v[134:135], off offset:256
	global_load_dwordx2 v[200:201], v[134:135], off offset:384
	global_load_dwordx2 v[202:203], v[134:135], off offset:1024
	global_load_dwordx2 v[204:205], v[134:135], off offset:1152
	global_load_dwordx2 v[206:207], v[134:135], off offset:1280
	global_load_dwordx2 v[208:209], v[134:135], off offset:1408
	s_mov_b32 s26, 0xff61b1e6
	s_waitcnt vmcnt(7)
	v_ffbh_u32_e32 v138, v195
	v_min_u32_e32 v138, 32, v138
	v_lshlrev_b64 v[136:137], v138, v[194:195]
	v_min_u32_e32 v136, 1, v136
	v_or_b32_e32 v136, v137, v136
	v_cvt_f32_u32_e32 v136, v136
	v_sub_u32_e32 v137, 32, v138
	v_ldexp_f32 v136, v136, v137
	v_fmamk_f32 v136, v136, 0x30000000, v250
	v_rsq_f32_e32 v136, v136
	s_nop 0
	v_pk_mul_f32 v[128:129], v[128:129], v[136:137] op_sel_hi:[1,0]
	v_pk_mul_f32 v[126:127], v[126:127], v[136:137] op_sel_hi:[1,0]
	v_max_f32_e32 v137, v128, v129
	v_max3_f32 v137, v126, v127, v137
	v_pk_mul_f32 v[124:125], v[124:125], v[136:137] op_sel_hi:[1,0]
	v_pk_mul_f32 v[122:123], v[122:123], v[136:137] op_sel_hi:[1,0]
	v_max_f32_e32 v138, v124, v125
	v_max3_f32 v138, v122, v123, v138
	v_max3_f32 v137, v137, s26, v138
	v_pk_mul_f32 v[170:171], v[120:121], v[136:137] op_sel_hi:[1,0]
	v_pk_mul_f32 v[174:175], v[116:117], v[136:137] op_sel_hi:[1,0]
	v_pk_mul_f32 v[176:177], v[118:119], v[136:137] op_sel_hi:[1,0]
	v_max_f32_e32 v118, v170, v171
	v_pk_mul_f32 v[116:117], v[114:115], v[136:137] op_sel_hi:[1,0]
	v_max_f32_e32 v114, v174, v175
	v_max3_f32 v118, v176, v177, v118
	v_max3_f32 v114, v116, v117, v114
	v_max3_f32 v114, v137, v118, v114
	ds_bpermute_b32 v115, v133, v114
	s_waitcnt lgkmcnt(0)
	v_max_f32_e32 v115, v115, v115
	v_max_f32_e32 v114, v114, v115
	ds_bpermute_b32 v115, v220, v114
	s_and_saveexec_b64 s[26:27], vcc
	s_cbranch_execz .LBB0_972
	s_waitcnt lgkmcnt(0)
	v_max_f32_e32 v115, v115, v115
	v_max_f32_e32 v114, v114, v114
	v_max_f32_e32 v114, v114, v115
	v_add_u32_e32 v115, 0, v221
	v_add_u32_e32 v115, 0x20400, v115
	ds_write_b32 v115, v114
.LBB0_972:
	s_or_b64 exec, exec, s[26:27]
	s_waitcnt lgkmcnt(0)
	s_mov_b32 s26, 0xff61b1e6
	s_waitcnt vmcnt(6)
	v_ffbh_u32_e32 v118, v197
	v_min_u32_e32 v118, 32, v118
	v_lshlrev_b64 v[114:115], v118, v[196:197]
	v_min_u32_e32 v114, 1, v114
	v_or_b32_e32 v114, v115, v114
	v_cvt_f32_u32_e32 v114, v114
	v_sub_u32_e32 v115, 32, v118
	v_ldexp_f32 v114, v114, v115
	v_fmamk_f32 v114, v114, 0x30000000, v250
	v_rsq_f32_e32 v114, v114
	s_nop 0
	v_pk_mul_f32 v[212:213], v[104:105], v[114:115] op_sel_hi:[1,0]
	v_pk_mul_f32 v[188:189], v[100:101], v[114:115] op_sel_hi:[1,0]
	v_pk_mul_f32 v[214:215], v[102:103], v[114:115] op_sel_hi:[1,0]
	v_pk_mul_f32 v[210:211], v[98:99], v[114:115] op_sel_hi:[1,0]
	v_pk_mul_f32 v[100:101], v[112:113], v[114:115] op_sel_hi:[1,0]
	v_pk_mul_f32 v[180:181], v[108:109], v[114:115] op_sel_hi:[1,0]
	v_max_f32_e32 v98, v212, v213
	v_max_f32_e32 v99, v188, v189
	v_pk_mul_f32 v[186:187], v[110:111], v[114:115] op_sel_hi:[1,0]
	v_pk_mul_f32 v[104:105], v[106:107], v[114:115] op_sel_hi:[1,0]
	v_max_f32_e32 v102, v100, v101
	v_max_f32_e32 v103, v180, v181
	v_max3_f32 v98, v214, v215, v98
	v_max3_f32 v99, v210, v211, v99
	v_max3_f32 v102, v186, v187, v102
	v_max3_f32 v98, v98, s26, v99
	v_max3_f32 v99, v104, v105, v103
	v_max3_f32 v98, v98, v102, v99
	ds_bpermute_b32 v99, v133, v98
	s_waitcnt lgkmcnt(0)
	v_max_f32_e32 v99, v99, v99
	v_max_f32_e32 v98, v98, v99
	ds_bpermute_b32 v99, v220, v98
	s_and_saveexec_b64 s[26:27], vcc
	s_cbranch_execz .LBB0_974
	s_waitcnt lgkmcnt(0)
	v_max_f32_e32 v99, v99, v99
	v_max_f32_e32 v98, v98, v98
	s_add_i32 s28, 0, 0x20400
	v_max_f32_e32 v98, v98, v99
	v_add_u32_e32 v99, s28, v221
	ds_write_b32 v99, v98 offset:256
.LBB0_974:
	s_or_b64 exec, exec, s[26:27]
	s_waitcnt lgkmcnt(0)
	s_mov_b32 s26, 0xff61b1e6
	s_waitcnt vmcnt(5)
	v_ffbh_u32_e32 v102, v199
	v_min_u32_e32 v102, 32, v102
	v_lshlrev_b64 v[98:99], v102, v[198:199]
	v_min_u32_e32 v98, 1, v98
	v_or_b32_e32 v98, v99, v98
	v_cvt_f32_u32_e32 v98, v98
	v_sub_u32_e32 v99, 32, v102
	v_ldexp_f32 v98, v98, v99
	v_fmamk_f32 v98, v98, 0x30000000, v250
	v_rsq_f32_e32 v98, v98
	s_nop 0
	v_pk_mul_f32 v[182:183], v[88:89], v[98:99] op_sel_hi:[1,0]
	v_pk_mul_f32 v[110:111], v[84:85], v[98:99] op_sel_hi:[1,0]
	v_pk_mul_f32 v[184:185], v[86:87], v[98:99] op_sel_hi:[1,0]
	v_pk_mul_f32 v[178:179], v[82:83], v[98:99] op_sel_hi:[1,0]
	v_pk_mul_f32 v[84:85], v[96:97], v[98:99] op_sel_hi:[1,0]
	v_pk_mul_f32 v[106:107], v[92:93], v[98:99] op_sel_hi:[1,0]
	v_max_f32_e32 v82, v182, v183
	v_max_f32_e32 v83, v110, v111
	v_pk_mul_f32 v[172:173], v[94:95], v[98:99] op_sel_hi:[1,0]
	v_pk_mul_f32 v[88:89], v[90:91], v[98:99] op_sel_hi:[1,0]
	v_max_f32_e32 v86, v84, v85
	v_max_f32_e32 v87, v106, v107
	v_max3_f32 v82, v184, v185, v82
	v_max3_f32 v83, v178, v179, v83
	v_max3_f32 v86, v172, v173, v86
	v_max3_f32 v82, v82, s26, v83
	v_max3_f32 v83, v88, v89, v87
	v_max3_f32 v82, v82, v86, v83
	ds_bpermute_b32 v83, v133, v82
	s_waitcnt lgkmcnt(0)
	v_max_f32_e32 v83, v83, v83
	v_max_f32_e32 v82, v82, v83
	ds_bpermute_b32 v83, v220, v82
	s_and_saveexec_b64 s[26:27], vcc
	s_cbranch_execz .LBB0_976
	s_waitcnt lgkmcnt(0)
	v_max_f32_e32 v83, v83, v83
	v_max_f32_e32 v82, v82, v82
	s_add_i32 s28, 0, 0x20400
	v_max_f32_e32 v82, v82, v83
	v_add_u32_e32 v83, s28, v221
	ds_write_b32 v83, v82 offset:512
.LBB0_976:
	s_or_b64 exec, exec, s[26:27]
	s_waitcnt lgkmcnt(0)
	s_mov_b32 s26, 0xff61b1e6
	s_waitcnt vmcnt(4)
	v_ffbh_u32_e32 v86, v201
	v_min_u32_e32 v86, 32, v86
	v_lshlrev_b64 v[82:83], v86, v[200:201]
	v_min_u32_e32 v82, 1, v82
	v_or_b32_e32 v82, v83, v82
	v_cvt_f32_u32_e32 v82, v82
	v_sub_u32_e32 v83, 32, v86
	v_ldexp_f32 v82, v82, v83
	v_fmamk_f32 v82, v82, 0x30000000, v250
	v_rsq_f32_e32 v82, v82
	s_nop 0
	v_pk_mul_f32 v[166:167], v[56:57], v[82:83] op_sel_hi:[1,0]
	v_pk_mul_f32 v[90:91], v[52:53], v[82:83] op_sel_hi:[1,0]
	v_pk_mul_f32 v[168:169], v[54:55], v[82:83] op_sel_hi:[1,0]
	v_pk_mul_f32 v[164:165], v[50:51], v[82:83] op_sel_hi:[1,0]
	v_pk_mul_f32 v[160:161], v[64:65], v[82:83] op_sel_hi:[1,0]
	v_pk_mul_f32 v[60:61], v[60:61], v[82:83] op_sel_hi:[1,0]
	v_max_f32_e32 v50, v166, v167
	v_max_f32_e32 v51, v90, v91
	v_pk_mul_f32 v[62:63], v[62:63], v[82:83] op_sel_hi:[1,0]
	v_pk_mul_f32 v[86:87], v[58:59], v[82:83] op_sel_hi:[1,0]
	v_max_f32_e32 v52, v160, v161
	v_max_f32_e32 v53, v60, v61
	v_max3_f32 v50, v168, v169, v50
	v_max3_f32 v51, v164, v165, v51
	v_max3_f32 v52, v62, v63, v52
	v_max3_f32 v50, v50, s26, v51
	v_max3_f32 v51, v86, v87, v53
	v_max3_f32 v50, v50, v52, v51
	ds_bpermute_b32 v51, v133, v50
	s_waitcnt lgkmcnt(0)
	v_max_f32_e32 v51, v51, v51
	v_max_f32_e32 v50, v50, v51
	ds_bpermute_b32 v51, v220, v50
	s_and_saveexec_b64 s[26:27], vcc
	s_cbranch_execz .LBB0_978
	s_waitcnt lgkmcnt(0)
	v_max_f32_e32 v51, v51, v51
	v_max_f32_e32 v50, v50, v50
	s_add_i32 s28, 0, 0x20400
	v_max_f32_e32 v50, v50, v51
	v_add_u32_e32 v51, s28, v221
	ds_write_b32 v51, v50 offset:768
.LBB0_978:
	s_or_b64 exec, exec, s[26:27]
	s_waitcnt lgkmcnt(0)
	s_mov_b32 s26, 0xff61b1e6
	s_waitcnt vmcnt(3)
	v_ffbh_u32_e32 v52, v203
	v_min_u32_e32 v52, 32, v52
	v_lshlrev_b64 v[50:51], v52, v[202:203]
	v_min_u32_e32 v50, 1, v50
	v_or_b32_e32 v50, v51, v50
	v_cvt_f32_u32_e32 v50, v50
	v_sub_u32_e32 v51, 32, v52
	v_ldexp_f32 v50, v50, v51
	v_fmamk_f32 v50, v50, 0x30000000, v250
	v_rsq_f32_e32 v52, v50
	s_nop 0
	v_pk_mul_f32 v[158:159], v[72:73], v[52:53] op_sel_hi:[1,0]
	v_pk_mul_f32 v[68:69], v[68:69], v[52:53] op_sel_hi:[1,0]
	v_pk_mul_f32 v[162:163], v[70:71], v[52:53] op_sel_hi:[1,0]
	v_pk_mul_f32 v[58:59], v[66:67], v[52:53] op_sel_hi:[1,0]
	v_pk_mul_f32 v[50:51], v[80:81], v[52:53] op_sel_hi:[1,0]
	v_pk_mul_f32 v[156:157], v[78:79], v[52:53] op_sel_hi:[1,0]
	v_pk_mul_f32 v[64:65], v[76:77], v[52:53] op_sel_hi:[1,0]
	v_pk_mul_f32 v[54:55], v[74:75], v[52:53] op_sel_hi:[1,0]
	v_max_f32_e32 v52, v158, v159
	v_max_f32_e32 v53, v68, v69
	v_max_f32_e32 v56, v50, v51
	v_max_f32_e32 v57, v64, v65
	v_max3_f32 v52, v162, v163, v52
	v_max3_f32 v53, v58, v59, v53
	v_max3_f32 v56, v156, v157, v56
	v_max3_f32 v52, v52, s26, v53
	v_max3_f32 v53, v54, v55, v57
	v_max3_f32 v52, v52, v56, v53
	ds_bpermute_b32 v53, v133, v52
	s_waitcnt lgkmcnt(0)
	v_max_f32_e32 v53, v53, v53
	v_max_f32_e32 v52, v52, v53
	ds_bpermute_b32 v53, v220, v52
	s_and_saveexec_b64 s[26:27], vcc
	s_cbranch_execz .LBB0_980
	s_waitcnt lgkmcnt(0)
	v_max_f32_e32 v53, v53, v53
	v_max_f32_e32 v52, v52, v52
	s_add_i32 s28, 0, 0x20400
	v_max_f32_e32 v52, v52, v53
	v_add_u32_e32 v53, s28, v221
	ds_write_b32 v53, v52 offset:2048
.LBB0_980:
	s_or_b64 exec, exec, s[26:27]
	s_waitcnt lgkmcnt(0)
	s_mov_b32 s26, 0xff61b1e6
	s_waitcnt vmcnt(2)
	v_ffbh_u32_e32 v56, v205
	v_min_u32_e32 v56, 32, v56
	v_lshlrev_b64 v[52:53], v56, v[204:205]
	v_min_u32_e32 v52, 1, v52
	v_or_b32_e32 v52, v53, v52
	v_cvt_f32_u32_e32 v52, v52
	v_sub_u32_e32 v53, 32, v56
	v_ldexp_f32 v52, v52, v53
	v_fmamk_f32 v52, v52, 0x30000000, v250
	v_rsq_f32_e32 v66, v52
	s_nop 0
	v_pk_mul_f32 v[152:153], v[40:41], v[66:67] op_sel_hi:[1,0]
	v_pk_mul_f32 v[56:57], v[36:37], v[66:67] op_sel_hi:[1,0]
	v_pk_mul_f32 v[154:155], v[38:39], v[66:67] op_sel_hi:[1,0]
	v_pk_mul_f32 v[150:151], v[34:35], v[66:67] op_sel_hi:[1,0]
	v_pk_mul_f32 v[34:35], v[48:49], v[66:67] op_sel_hi:[1,0]
	v_pk_mul_f32 v[52:53], v[44:45], v[66:67] op_sel_hi:[1,0]
	v_max_f32_e32 v36, v152, v153
	v_max_f32_e32 v37, v56, v57
	v_pk_mul_f32 v[148:149], v[46:47], v[66:67] op_sel_hi:[1,0]
	v_pk_mul_f32 v[40:41], v[42:43], v[66:67] op_sel_hi:[1,0]
	v_max_f32_e32 v38, v34, v35
	v_max_f32_e32 v39, v52, v53
	v_max3_f32 v36, v154, v155, v36
	v_max3_f32 v37, v150, v151, v37
	v_max3_f32 v38, v148, v149, v38
	v_max3_f32 v36, v36, s26, v37
	v_max3_f32 v37, v40, v41, v39
	v_max3_f32 v36, v36, v38, v37
	ds_bpermute_b32 v37, v133, v36
	s_waitcnt lgkmcnt(0)
	v_max_f32_e32 v37, v37, v37
	v_max_f32_e32 v36, v36, v37
	ds_bpermute_b32 v37, v220, v36
	s_and_saveexec_b64 s[26:27], vcc
	s_cbranch_execz .LBB0_982
	s_waitcnt lgkmcnt(0)
	v_max_f32_e32 v37, v37, v37
	v_max_f32_e32 v36, v36, v36
	s_add_i32 s28, 0, 0x20400
	v_max_f32_e32 v36, v36, v37
	v_add_u32_e32 v37, s28, v221
	ds_write_b32 v37, v36 offset:2304
.LBB0_982:
	s_or_b64 exec, exec, s[26:27]
	s_waitcnt lgkmcnt(0)
	s_mov_b32 s26, 0xff61b1e6
	s_waitcnt vmcnt(1)
	v_ffbh_u32_e32 v38, v207
	v_min_u32_e32 v38, 32, v38
	v_lshlrev_b64 v[36:37], v38, v[206:207]
	v_min_u32_e32 v36, 1, v36
	v_or_b32_e32 v36, v37, v36
	v_cvt_f32_u32_e32 v36, v36
	v_sub_u32_e32 v37, 32, v38
	v_ldexp_f32 v36, v36, v37
	v_fmamk_f32 v36, v36, 0x30000000, v250
	v_rsq_f32_e32 v36, v36
	s_nop 0
	v_pk_mul_f32 v[144:145], v[24:25], v[36:37] op_sel_hi:[1,0]
	v_pk_mul_f32 v[42:43], v[20:21], v[36:37] op_sel_hi:[1,0]
	v_pk_mul_f32 v[146:147], v[22:23], v[36:37] op_sel_hi:[1,0]
	v_pk_mul_f32 v[142:143], v[18:19], v[36:37] op_sel_hi:[1,0]
	v_pk_mul_f32 v[20:21], v[32:33], v[36:37] op_sel_hi:[1,0]
	v_pk_mul_f32 v[38:39], v[28:29], v[36:37] op_sel_hi:[1,0]
	v_max_f32_e32 v18, v144, v145
	v_max_f32_e32 v19, v42, v43
	v_pk_mul_f32 v[140:141], v[30:31], v[36:37] op_sel_hi:[1,0]
	v_pk_mul_f32 v[26:27], v[26:27], v[36:37] op_sel_hi:[1,0]
	v_max_f32_e32 v22, v20, v21
	v_max_f32_e32 v23, v38, v39
	v_max3_f32 v18, v146, v147, v18
	v_max3_f32 v19, v142, v143, v19
	v_max3_f32 v22, v140, v141, v22
	v_max3_f32 v18, v18, s26, v19
	v_max3_f32 v19, v26, v27, v23
	v_max3_f32 v18, v18, v22, v19
	ds_bpermute_b32 v19, v133, v18
	s_waitcnt lgkmcnt(0)
	v_max_f32_e32 v19, v19, v19
	v_max_f32_e32 v18, v18, v19
	ds_bpermute_b32 v19, v220, v18
	s_and_saveexec_b64 s[26:27], vcc
	s_cbranch_execz .LBB0_984
	s_waitcnt lgkmcnt(0)
	v_max_f32_e32 v19, v19, v19
	v_max_f32_e32 v18, v18, v18
	s_add_i32 s28, 0, 0x20400
	v_max_f32_e32 v18, v18, v19
	v_add_u32_e32 v19, s28, v221
	ds_write_b32 v19, v18 offset:2560
.LBB0_984:
	s_or_b64 exec, exec, s[26:27]
	s_waitcnt lgkmcnt(0)
	s_mov_b32 s26, 0xff61b1e6
	s_waitcnt vmcnt(0)
	v_ffbh_u32_e32 v22, v209
	v_min_u32_e32 v22, 32, v22
	v_lshlrev_b64 v[18:19], v22, v[208:209]
	v_min_u32_e32 v18, 1, v18
	v_or_b32_e32 v18, v19, v18
	v_cvt_f32_u32_e32 v18, v18
	v_sub_u32_e32 v19, 32, v22
	v_ldexp_f32 v18, v18, v19
	v_fmamk_f32 v18, v18, 0x30000000, v250
	v_rsq_f32_e32 v22, v18
	s_nop 0
	v_pk_mul_f32 v[136:137], v[8:9], v[22:23] op_sel_hi:[1,0]
	v_pk_mul_f32 v[24:25], v[4:5], v[22:23] op_sel_hi:[1,0]
	v_pk_mul_f32 v[138:139], v[6:7], v[22:23] op_sel_hi:[1,0]
	v_pk_mul_f32 v[134:135], v[2:3], v[22:23] op_sel_hi:[1,0]
	v_pk_mul_f32 v[6:7], v[16:17], v[22:23] op_sel_hi:[1,0]
	v_pk_mul_f32 v[18:19], v[12:13], v[22:23] op_sel_hi:[1,0]
	v_max_f32_e32 v4, v136, v137
	v_max_f32_e32 v5, v24, v25
	v_pk_mul_f32 v[2:3], v[14:15], v[22:23] op_sel_hi:[1,0]
	v_pk_mul_f32 v[8:9], v[10:11], v[22:23] op_sel_hi:[1,0]
	v_max_f32_e32 v10, v6, v7
	v_max_f32_e32 v11, v18, v19
	v_max3_f32 v4, v138, v139, v4
	v_max3_f32 v5, v134, v135, v5
	v_max3_f32 v10, v2, v3, v10
	v_max3_f32 v4, v4, s26, v5
	v_max3_f32 v5, v8, v9, v11
	v_max3_f32 v4, v4, v10, v5
	ds_bpermute_b32 v5, v133, v4
	s_waitcnt lgkmcnt(0)
	v_max_f32_e32 v5, v5, v5
	v_max_f32_e32 v4, v4, v5
	ds_bpermute_b32 v5, v220, v4
	s_and_saveexec_b64 s[26:27], vcc
	s_cbranch_execz .LBB0_986
	s_waitcnt lgkmcnt(0)
	v_max_f32_e32 v5, v5, v5
	v_max_f32_e32 v4, v4, v4
	s_add_i32 s28, 0, 0x20400
	v_max_f32_e32 v4, v4, v5
	v_add_u32_e32 v5, s28, v221
	ds_write_b32 v5, v4 offset:2816
